# tail scheme: only workgroups whose next DN unit really reads tail rows poll+invalidate
# speedup vs baseline: 1.0392x; 1.0221x over previous
; #define LAS __attribute__((address_space(3)))
;     __device__ __forceinline__ bool next(int i, Unit& u) const {
;         int U = i * G + c, e = 0, found = 0, rem = 0;
;         typedef int i32x4 __attribute__((ext_vector_type(4)));
;         const i32x4 c0 = *(const LAS i32x4*)(seg), c1 = *(const LAS i32x4*)(seg + 4), c2 = *(const LAS i32x4*)(seg + 8), c3 = *(const LAS i32x4*)(seg + 12);
; #pragma unroll
;         for (int k = 0; k < 16; ++k) { const int ck = k < 4 ? c0[k & 3] : k < 8 ? c1[k & 3] : k < 12 ? c2[k & 3] : c3[k & 3];
;             const int nu = ((ck + 255) >> 8) * nct; if (!found) { if (U < nu) { found = 1; e = k; rem = U; } else U -= nu; } }
;         if (!found) return false;
;         e = __builtin_amdgcn_readfirstlane(e); rem = __builtin_amdgcn_readfirstlane(rem);
;         const int rt = rem / nct, ct = rem % nct;
;         u.e = e; u.pm = rt; u.pn = ct; u.rows = seg[e] - rt * 256;
;         u.a = A + (size_t)(seg[16 + e] + rt * 256) * arow_bytes; u.b = Bt + (size_t)e * bexp_bytes + (size_t)ct * btile_bytes; return true;
;     __device__ __forceinline__ void pre(LAS unsigned char* lds, const pg8::Unit& u, int tid) const {
;         const int t = tid & 255, wv = __builtin_amdgcn_readfirstlane(tid >> 6);
;         const void* src = tid < 256 ? (const void*)(list + u.e * NTOK + u.pm * 256 + t) : (const void*)(listw + u.e * NTOK + u.pm * 256 + t);
;         lds_dma4(src, (unsigned)__builtin_amdgcn_readfirstlane((unsigned)(uintptr_t)lds + DNSL_OFF + u.par * 2048 + wv * 256));
;     }
.LBB0_1230:
	s_or_b64 exec, exec, s[24:25]
	s_lshl_b32 s8, s49, 11
	s_and_b32 s8, s8, 0x800
	s_lshl_b32 s9, s26, 2
	s_and_b32 s9, s9, 0xffffff00
	s_add_i32 s54, s8, 0
	s_add_i32 s8, s54, s9
	s_add_i32 s8, s8, 0x22400
	s_mov_b32 s9, m0
	s_mov_b32 m0, s8
	s_nop 0
	global_load_lds_dword v[36:37], off
	s_mov_b32 m0, s9
	v_mov_b32_e32 v34, s42
	ds_read_b128 v[134:137], v34
	s_add_i32 s23, s49, 1
	s_mul_i32 s8, s23, s77
	s_add_i32 s9, s8, s61
	s_cmp_lt_u32 s23, 3
	s_cbranch_scc1 .Ldn_perm_done
	v_readlane_b32 s24, v254, 63
	s_nop 1
	s_cmp_lt_u32 s61, s24
	s_cbranch_scc1 .Ldn_perm_bad
	s_sub_i32 s25, s77, s24
	s_add_i32 s26, s23, -3
	s_mul_i32 s25, s25, s26
	s_sub_i32 s26, s61, s24
	s_add_i32 s25, s25, s26
	s_mul_i32 s26, s77, 3
	s_add_i32 s9, s25, s26
	s_lshl_b32 s26, s77, 2
	s_cmp_lt_u32 s9, s26
	s_cbranch_scc1 .Ldn_perm_done
	s_add_i32 s26, s26, s24
	s_cmp_ge_u32 s9, s26
	s_cbranch_scc1 .Ldn_perm_done
	v_readlane_b32 s27, v254, 20
	s_nop 1
	s_lshl_b32 s27, s27, 2
	s_add_u32 s27, s27, 0x18000
	s_add_u32 s28, s92, s27
	s_addc_u32 s29, s93, 0
	v_mov_b32_e32 v138, 0
	s_mov_b32 s30, 0
